# speedup vs baseline: 1.0322x; 1.0092x over previous
.LBB1_28:
	s_or_b64 exec, exec, s[6:7]
	s_load_dwordx2 s[4:5], s[0:1], 0x8
	v_and_b32_e32 v174, 63, v244
	v_lshrrev_b32_e32 v170, 6, v244
	v_mov_b32_e32 v181, 0
	v_lshlrev_b32_e32 v180, 4, v174
	s_waitcnt lgkmcnt(0)
	v_lshl_add_u64 v[0:1], s[4:5], 0, v[180:181]
	v_mul_u32_u24_e32 v120, 0x1800, v170
	v_mov_b32_e32 v121, v181
	v_lshl_add_u64 v[2:3], v[0:1], 0, v[120:121]
	v_add_co_u32_e32 v4, vcc, 0x6000, v2
	s_mov_b64 s[4:5], 0x1000
	s_nop 0
	v_addc_co_u32_e32 v5, vcc, 0, v3, vcc
	v_add_co_u32_e32 v110, vcc, 0x1000, v2
	global_load_dwordx4 a[8:11], v[2:3], off
	global_load_dwordx4 a[12:15], v[2:3], off offset:1024
	global_load_dwordx4 a[16:19], v[4:5], off
	global_load_dwordx4 a[20:23], v[4:5], off offset:1024
	global_load_dwordx4 a[24:27], v[2:3], off offset:2048
	global_load_dwordx4 a[28:31], v[2:3], off offset:3072
	global_load_dwordx4 a[32:35], v[4:5], off offset:2048
	global_load_dwordx4 a[36:39], v[4:5], off offset:3072
	v_addc_co_u32_e32 v111, vcc, 0, v3, vcc
	v_add_co_u32_e32 v112, vcc, 0x7000, v2
	v_lshl_add_u64 v[4:5], v[2:3], 0, s[4:5]
	s_nop 0
	v_addc_co_u32_e32 v113, vcc, 0, v3, vcc
	global_load_dwordx4 a[40:43], v[110:111], off
	global_load_dwordx4 a[44:47], v[110:111], off offset:1024
	global_load_dwordx4 a[48:51], v[112:113], off
	global_load_dwordx4 a[52:55], v[112:113], off offset:1024
	v_add_co_u32_e32 v110, vcc, 0x18000, v2
	s_mov_b64 s[4:5], 0x1400
	s_nop 0
	v_addc_co_u32_e32 v111, vcc, 0, v3, vcc
	v_lshl_add_u64 v[114:115], v[2:3], 0, s[4:5]
	v_add_co_u32_e32 v2, vcc, 0x19000, v2
	v_mul_u32_u24_e32 v122, 0x3000, v170
	v_mov_b32_e32 v123, v181
	v_addc_co_u32_e32 v3, vcc, 0, v3, vcc
	v_lshl_add_u64 v[0:1], v[0:1], 0, v[122:123]
	global_load_dwordx4 a[56:59], v[110:111], off
	global_load_dwordx4 a[60:63], v[110:111], off offset:1024
	global_load_dwordx4 a[64:67], v[110:111], off offset:2048
	global_load_dwordx4 a[68:71], v[110:111], off offset:3072
	global_load_dwordx4 a[72:75], v[2:3], off
	global_load_dwordx4 a[76:79], v[2:3], off offset:1024
	v_add_co_u32_e32 v2, vcc, 0x48000, v0
	v_lshl_add_u64 v[144:145], v[4:5], 0, v[120:121]
	s_nop 0
	v_addc_co_u32_e32 v3, vcc, 0, v1, vcc
	global_load_dwordx4 a[80:83], v[2:3], off
	global_load_dwordx4 a[84:87], v[2:3], off offset:1024
	global_load_dwordx4 a[88:91], v[2:3], off offset:2048
	global_load_dwordx4 a[92:95], v[2:3], off offset:3072
	v_add_co_u32_e32 v2, vcc, 0x48000, v144
	v_lshl_add_u64 v[152:153], v[114:115], 0, v[120:121]
	s_nop 0
	v_addc_co_u32_e32 v3, vcc, 0, v145, vcc
	v_add_co_u32_e32 v4, vcc, 0x48000, v152
	s_mov_b32 s3, 0x30000
	s_nop 0
	v_addc_co_u32_e32 v5, vcc, 0, v153, vcc
	global_load_dwordx4 a[96:99], v[2:3], off
	global_load_dwordx4 a[100:103], v[4:5], off
	v_add_co_u32_e32 v2, vcc, 0x49000, v0
	v_mul_u32_u24_e32 v182, 0x6000, v170
	s_nop 0
	v_addc_co_u32_e32 v3, vcc, 0, v1, vcc
	global_load_dwordx4 a[104:107], v[2:3], off offset:2048
	global_load_dwordx4 a[108:111], v[2:3], off offset:3072
	v_add_co_u32_e32 v2, vcc, 0x4a000, v0
	v_or_b32_e32 v187, v182, v180
	s_nop 0
	v_readfirstlane_b32 s80, v187
	s_add_u32 s80, s80, 0xf010
	v_addc_co_u32_e32 v3, vcc, 0, v1, vcc
	v_add_co_u32_e32 v132, vcc, 0x30000, v0
	global_load_dwordx4 a[112:115], v[2:3], off
	global_load_dwordx4 a[116:119], v[2:3], off offset:1024
	global_load_dwordx4 a[120:123], v[2:3], off offset:2048
	global_load_dwordx4 a[124:127], v[2:3], off offset:3072
	v_addc_co_u32_e32 v133, vcc, 0, v1, vcc
	v_add_co_u32_e32 v140, vcc, 0x3c000, v0
	v_add_u32_e32 v188, 0xf010, v187
	s_nop 0
	v_addc_co_u32_e32 v141, vcc, 0, v1, vcc
	v_add_co_u32_e32 v144, vcc, s3, v144
	s_add_u32 m0, s80, 0x0
	s_nop 0
	global_load_lds_dwordx4 v[132:133], off
	s_add_u32 m0, s80, 0x400
	s_nop 0
	global_load_lds_dwordx4 v[132:133], off offset:1024
	s_add_u32 m0, s80, 0x400
	s_nop 0
	global_load_lds_dwordx4 v[140:141], off
	s_add_u32 m0, s80, 0x800
	s_nop 0
	global_load_lds_dwordx4 v[140:141], off offset:1024
	s_add_u32 m0, s80, 0x800
	s_nop 0
	global_load_lds_dwordx4 v[132:133], off offset:2048
	s_nop 0
	s_add_u32 m0, s80, 0xc00
	s_nop 0
	global_load_lds_dwordx4 v[132:133], off offset:3072
	s_nop 0
	s_add_u32 m0, s80, 0xc00
	s_nop 0
	global_load_lds_dwordx4 v[140:141], off offset:2048
	s_nop 0
	s_add_u32 m0, s80, 0x1000
	s_nop 0
	global_load_lds_dwordx4 v[140:141], off offset:3072
	v_addc_co_u32_e32 v145, vcc, 0, v145, vcc
	v_add_co_u32_e32 v168, vcc, 0x3d000, v0
	s_nop 1
	v_addc_co_u32_e32 v169, vcc, 0, v1, vcc
	v_add_co_u32_e32 v172, vcc, s3, v152
	s_add_u32 m0, s80, 0x2000
	s_nop 0
	global_load_lds_dwordx4 v[144:145], off
	s_nop 0
	s_add_u32 m0, s80, 0x2400
	s_nop 0
	global_load_lds_dwordx4 v[168:169], off
	v_addc_co_u32_e32 v173, vcc, 0, v153, vcc
	v_add_co_u32_e32 v164, vcc, 0x31000, v0
	s_nop 1
	v_addc_co_u32_e32 v165, vcc, 0, v1, vcc
	s_add_u32 m0, s80, 0x2800
	s_nop 0
	global_load_lds_dwordx4 v[168:169], off offset:1024
	s_add_u32 m0, s80, 0x2c00
	s_nop 0
	global_load_lds_dwordx4 v[168:169], off offset:2048
	s_add_u32 m0, s80, 0x2800
	s_nop 0
	global_load_lds_dwordx4 v[164:165], off offset:2048
	s_nop 0
	s_add_u32 m0, s80, 0x2c00
	s_nop 0
	global_load_lds_dwordx4 v[164:165], off offset:3072
	s_nop 0
	s_add_u32 m0, s80, 0x2800
	s_nop 0
	global_load_lds_dwordx4 v[172:173], off
	s_add_u32 m0, s80, 0x3000
	s_nop 0
	global_load_lds_dwordx4 v[168:169], off offset:3072
	v_add_co_u32_e32 v168, vcc, 0x32000, v0
	s_nop 1
	v_addc_co_u32_e32 v169, vcc, 0, v1, vcc
	v_add_co_u32_e32 v0, vcc, 0x3e000, v0
	s_nop 1
	v_addc_co_u32_e32 v1, vcc, 0, v1, vcc
	s_add_u32 m0, s80, 0x4000
	s_nop 0
	global_load_lds_dwordx4 v[168:169], off
	s_add_u32 m0, s80, 0x4400
	s_nop 0
	global_load_lds_dwordx4 v[168:169], off offset:1024
	s_add_u32 m0, s80, 0x4400
	s_nop 0
	global_load_lds_dwordx4 v[0:1], off
	s_add_u32 m0, s80, 0x4800
	s_nop 0
	global_load_lds_dwordx4 v[0:1], off offset:1024
	s_add_u32 m0, s80, 0x4800
	s_nop 0
	global_load_lds_dwordx4 v[168:169], off offset:2048
	s_add_u32 m0, s80, 0x4c00
	s_nop 0
	global_load_lds_dwordx4 v[168:169], off offset:3072
	s_add_u32 m0, s80, 0x4c00
	s_nop 0
	global_load_lds_dwordx4 v[0:1], off offset:2048
	s_add_u32 m0, s80, 0x5000
	s_nop 0
	global_load_lds_dwordx4 v[0:1], off offset:3072
	v_or_b32_e32 v2, 0xffffff00, v244
	v_lshlrev_b32_e32 v3, 4, v244
	s_mov_b64 s[4:5], 0
	v_mov_b32_e32 v110, v181
	v_mov_b32_e32 v111, v181
	v_mov_b32_e32 v112, v181
	v_mov_b32_e32 v113, v181
	s_movk_i32 s3, 0x780

.LBB1_75:
	s_cmp_lg_u32 s25, 12
	s_cbranch_scc1 .LBB1_77
	v_accvgpr_read_b32 v0, a146
	v_accvgpr_read_b32 v1, a147
	global_load_dwordx4 a[8:11], v[62:63], off
	global_load_dwordx4 a[12:15], v[62:63], off offset:1024
	global_load_dwordx4 a[16:19], v[0:1], off
	v_accvgpr_read_b32 v0, a148
	v_accvgpr_read_b32 v1, a149
	global_load_dwordx4 a[20:23], v[0:1], off
	global_load_dwordx4 a[24:27], v[62:63], off offset:2048
	global_load_dwordx4 a[28:31], v[62:63], off offset:3072
	v_accvgpr_read_b32 v0, a150
	v_accvgpr_read_b32 v1, a151
	global_load_dwordx4 a[32:35], v[0:1], off
	v_accvgpr_read_b32 v0, a152
	v_accvgpr_read_b32 v1, a153
	global_load_dwordx4 a[36:39], v[0:1], off
	global_load_dwordx4 a[40:43], v[222:223], off
	v_accvgpr_read_b32 v0, a154
	v_accvgpr_read_b32 v1, a155
	global_load_dwordx4 a[48:51], v[0:1], off
	global_load_dwordx4 a[44:47], v[76:77], off
	v_accvgpr_read_b32 v0, a156
	v_accvgpr_read_b32 v1, a157
	global_load_dwordx4 a[52:55], v[0:1], off
	v_accvgpr_read_b32 v0, a158
	v_accvgpr_read_b32 v1, a159
	global_load_dwordx4 a[56:59], v[0:1], off
	v_accvgpr_read_b32 v0, a160
	v_accvgpr_read_b32 v1, a161
	global_load_dwordx4 a[60:63], v[0:1], off
	v_accvgpr_read_b32 v0, a162
	v_accvgpr_read_b32 v1, a163
	global_load_dwordx4 a[64:67], v[0:1], off
	v_accvgpr_read_b32 v0, a164
	v_accvgpr_read_b32 v1, a165
	global_load_dwordx4 a[68:71], v[0:1], off
	v_accvgpr_read_b32 v0, a166
	v_accvgpr_read_b32 v1, a167
	global_load_dwordx4 a[72:75], v[0:1], off
	v_accvgpr_read_b32 v0, a168
	v_accvgpr_read_b32 v1, a169
	global_load_dwordx4 a[76:79], v[0:1], off
	v_accvgpr_read_b32 v0, a170
	v_accvgpr_read_b32 v1, a171
	global_load_dwordx4 a[80:83], v[0:1], off
	v_accvgpr_read_b32 v0, a172
	v_accvgpr_read_b32 v1, a173
	global_load_dwordx4 a[84:87], v[0:1], off
	v_accvgpr_read_b32 v0, a174
	v_accvgpr_read_b32 v1, a175
	global_load_dwordx4 a[88:91], v[0:1], off
	v_accvgpr_read_b32 v0, a176
	v_accvgpr_read_b32 v1, a177
	global_load_dwordx4 a[92:95], v[0:1], off
	v_accvgpr_read_b32 v0, a178
	v_accvgpr_read_b32 v1, a179
	global_load_dwordx4 a[96:99], v[0:1], off
	v_accvgpr_read_b32 v0, a180
	v_accvgpr_read_b32 v1, a181
	global_load_dwordx4 a[100:103], v[0:1], off
	v_accvgpr_read_b32 v0, a182
	v_accvgpr_read_b32 v1, a183
	global_load_dwordx4 a[104:107], v[0:1], off
	v_accvgpr_read_b32 v0, a184
	v_accvgpr_read_b32 v1, a185
	global_load_dwordx4 a[108:111], v[0:1], off
	v_accvgpr_read_b32 v0, a186
	v_accvgpr_read_b32 v1, a187
	global_load_dwordx4 a[112:115], v[0:1], off
	v_accvgpr_read_b32 v0, a188
	v_accvgpr_read_b32 v1, a189
	global_load_dwordx4 a[116:119], v[0:1], off
	v_accvgpr_read_b32 v0, a190
	v_accvgpr_read_b32 v1, a191
	global_load_dwordx4 a[120:123], v[0:1], off
	v_accvgpr_read_b32 v0, a192
	v_accvgpr_read_b32 v1, a193
	global_load_dwordx4 a[124:127], v[0:1], off
	v_accvgpr_read_b32 v0, a194
	v_accvgpr_read_b32 v1, a195
	s_add_u32 m0, s80, 0x0
	s_nop 0
	global_load_lds_dwordx4 v[0:1], off
	v_accvgpr_read_b32 v0, a196
	v_accvgpr_read_b32 v1, a197
	s_add_u32 m0, s80, 0x400
	s_nop 0
	global_load_lds_dwordx4 v[0:1], off
	v_accvgpr_read_b32 v0, a198
	v_accvgpr_read_b32 v1, a199
	s_add_u32 m0, s80, 0x800
	s_nop 0
	global_load_lds_dwordx4 v[0:1], off
	v_accvgpr_read_b32 v0, a200
	v_accvgpr_read_b32 v1, a201
	s_add_u32 m0, s80, 0xc00
	s_nop 0
	global_load_lds_dwordx4 v[0:1], off
	v_accvgpr_read_b32 v0, a202
	v_accvgpr_read_b32 v1, a203
	s_add_u32 m0, s80, 0x1000
	s_nop 0
	global_load_lds_dwordx4 v[0:1], off
	v_accvgpr_read_b32 v0, a204
	v_accvgpr_read_b32 v1, a205
	s_add_u32 m0, s80, 0x1400
	s_nop 0
	global_load_lds_dwordx4 v[0:1], off
	v_accvgpr_read_b32 v0, a206
	v_accvgpr_read_b32 v1, a207
	s_add_u32 m0, s80, 0x1800
	s_nop 0
	global_load_lds_dwordx4 v[0:1], off
	v_accvgpr_read_b32 v0, a208
	v_accvgpr_read_b32 v1, a209
	s_add_u32 m0, s80, 0x1c00
	s_nop 0
	global_load_lds_dwordx4 v[0:1], off
	v_accvgpr_read_b32 v0, a210
	v_accvgpr_read_b32 v1, a211
	s_add_u32 m0, s80, 0x2000
	s_nop 0
	global_load_lds_dwordx4 v[0:1], off
	v_accvgpr_read_b32 v0, a212
	v_accvgpr_read_b32 v1, a213
	s_add_u32 m0, s80, 0x2400
	s_nop 0
	global_load_lds_dwordx4 v[0:1], off
	v_accvgpr_read_b32 v0, a214
	v_accvgpr_read_b32 v1, a215
	s_add_u32 m0, s80, 0x2800
	s_nop 0
	global_load_lds_dwordx4 v[0:1], off
	v_accvgpr_read_b32 v0, a216
	v_accvgpr_read_b32 v1, a217
	s_add_u32 m0, s80, 0x2c00
	s_nop 0
	global_load_lds_dwordx4 v[0:1], off
	v_accvgpr_read_b32 v0, a218
	v_accvgpr_read_b32 v1, a219
	s_add_u32 m0, s80, 0x3000
	s_nop 0
	global_load_lds_dwordx4 v[0:1], off
	v_accvgpr_read_b32 v0, a220
	v_accvgpr_read_b32 v1, a221
	s_add_u32 m0, s80, 0x3400
	s_nop 0
	global_load_lds_dwordx4 v[0:1], off
	v_accvgpr_read_b32 v0, a222
	v_accvgpr_read_b32 v1, a223
	s_add_u32 m0, s80, 0x3800
	s_nop 0
	global_load_lds_dwordx4 v[0:1], off
	v_accvgpr_read_b32 v0, a224
	v_accvgpr_read_b32 v1, a225
	s_add_u32 m0, s80, 0x3c00
	s_nop 0
	global_load_lds_dwordx4 v[0:1], off
	v_accvgpr_read_b32 v0, a226
	v_accvgpr_read_b32 v1, a227
	s_add_u32 m0, s80, 0x4000
	s_nop 0
	global_load_lds_dwordx4 v[0:1], off
	v_accvgpr_read_b32 v0, a228
	v_accvgpr_read_b32 v1, a229
	s_add_u32 m0, s80, 0x4400
	s_nop 0
	global_load_lds_dwordx4 v[0:1], off
	v_accvgpr_read_b32 v0, a230
	v_accvgpr_read_b32 v1, a231
	s_add_u32 m0, s80, 0x4800
	s_nop 0
	global_load_lds_dwordx4 v[0:1], off
	v_accvgpr_read_b32 v0, a232
	v_accvgpr_read_b32 v1, a233
	s_add_u32 m0, s80, 0x4c00
	s_nop 0
	global_load_lds_dwordx4 v[0:1], off
	v_accvgpr_read_b32 v0, a234
	v_accvgpr_read_b32 v1, a235
	s_add_u32 m0, s80, 0x5000
	s_nop 0
	global_load_lds_dwordx4 v[0:1], off
	v_accvgpr_read_b32 v0, a236
	v_accvgpr_read_b32 v1, a237
	s_add_u32 m0, s80, 0x5400
	s_nop 0
	global_load_lds_dwordx4 v[0:1], off
	s_add_u32 m0, s80, 0x5800
	s_nop 0
	global_load_lds_dwordx4 v[4:5], off
	s_add_u32 m0, s80, 0x5c00
	s_nop 0
	global_load_lds_dwordx4 v[166:167], off
	s_waitcnt vmcnt(24)
